# speedup vs baseline: 1.0064x; 1.0064x over previous
_Z11attn_kernelPKDF16_S0_S0_PfPDF16_S1_:
	s_lshl_b32 s3, s2, 7
	s_lshr_b32 s4, s2, 2
	s_and_b32 s3, s3, 0x180
	s_and_b32 s4, s4, 0x3ffffffe
	s_add_i32 s3, s3, s4
	s_bfe_u32 s2, s2, 0x10002
	s_or_b32 s40, s3, s2
	s_mov_b32 s41, 0
	s_lshl_b64 s[2:3], s[40:41], 2
	s_getpc_b64 s[4:5]
	s_add_u32 s4, s4, g_tab@rel32@lo+4
	s_addc_u32 s5, s5, g_tab@rel32@hi+12
	s_add_u32 s42, s4, s2
	s_addc_u32 s43, s5, s3
	s_load_dword s12, s[42:43], 0x0
	s_load_dwordx4 s[4:7], s[0:1], 0x8
	v_lshlrev_b32_e32 v2, 4, v0
	s_movk_i32 s8, 0x70
	v_readfirstlane_b32 s3, v0
	s_waitcnt lgkmcnt(0)
	s_add_u32 s70, s4, 0x2000
	s_addc_u32 s71, s5, 0
	s_add_u32 s72, s6, 0x2000
	s_addc_u32 s73, s7, 0
	s_and_b32 s2, s12, 3
	s_lshl_b32 s10, s2, 19
	v_bitop3_b32 v10, v2, s8, v0 bitop3:0x48
	s_add_u32 s8, s6, s10
	s_addc_u32 s9, s7, 0
	s_lshr_b32 s13, s3, 6
	s_bfe_u32 s40, s12, 0x70007
	s_bfe_u32 s33, s12, 0x6000e
	v_and_b32_e32 v1, 0x1f80, v2
	s_add_u32 s10, s4, s10
	v_or_b32_e32 v50, v10, v1
	v_mov_b32_e32 v51, 0
	s_addc_u32 s11, s5, 0
	v_lshl_add_u64 v[52:53], s[10:11], 0, v[50:51]
	v_lshl_add_u64 v[54:55], s[8:9], 0, v[50:51]
	s_lshl_b32 s8, s40, 13
	s_mov_b32 s9, s41
	s_lshl_b32 s50, s13, 10
	v_lshl_add_u64 v[2:3], v[52:53], 0, s[8:9]
	s_mov_b32 m0, s50
	s_add_i32 s51, s50, 0x2000
	global_load_lds_dwordx4 v[2:3], off
	v_lshl_add_u64 v[2:3], v[54:55], 0, s[8:9]
	s_mov_b32 m0, s51
	s_cmp_eq_u32 s33, 0
	global_load_lds_dwordx4 v[2:3], off
	s_cbranch_scc1 .LBB2_30
	s_load_dwordx2 s[14:15], s[0:1], 0x0
	s_load_dwordx4 s[8:11], s[0:1], 0x18
	s_load_dwordx2 s[44:45], s[0:1], 0x28
	s_lshl_b32 s52, s13, 4
	s_lshl_b32 s0, s2, 12
	v_and_b32_e32 v56, 15, v0
	v_bfe_u32 v15, v0, 4, 2
	v_lshrrev_b32_e32 v14, 1, v0
	v_bfe_u32 v2, v0, 1, 3
	s_add_i32 s54, s52, s0
	v_lshlrev_b32_e32 v16, 7, v56
	v_bitop3_b32 v3, v15, v14, 7 bitop3:0x78
	v_bitop3_b32 v2, v15, v2, 4 bitop3:0x36
	s_bfe_u32 s53, s12, 0x50002
	v_or_b32_e32 v18, s54, v56
	v_lshl_or_b32 v57, v3, 4, v16
	v_lshl_or_b32 v81, v2, 4, v16
	v_lshl_add_u32 v2, s53, 7, v18
	v_mov_b32_e32 v3, v51
	v_lshlrev_b64 v[2:3], 7, v[2:3]
	v_and_b32_e32 v50, 48, v0
	s_waitcnt lgkmcnt(0)
	v_lshl_add_u64 v[2:3], s[14:15], 0, v[2:3]
	v_lshl_add_u64 v[12:13], v[2:3], 0, v[50:51]
	global_load_dwordx4 v[2:5], v[12:13], off offset:64
	global_load_dwordx4 v[6:9], v[12:13], off
	v_and_b32_e32 v11, 63, v0
	v_bfe_u32 v12, v0, 5, 1
	s_mulk_i32 s13, 0xc00
	v_and_b32_e32 v13, 7, v0
	v_cmp_gt_u32_e64 s[0:1], 16, v11
	v_bitop3_b32 v11, v12, v0, 7 bitop3:0x78
	s_lshr_b32 s55, s3, 8
	s_add_i32 s3, s50, s13
	v_and_b32_e32 v14, 8, v14
	v_lshlrev_b32_e32 v23, 4, v11
	v_bitop3_b32 v11, v12, v13, 2 bitop3:0x36
	v_add3_u32 v19, s3, v16, v14
	v_bfe_u32 v14, v0, 3, 3
	v_lshlrev_b32_e32 v24, 4, v11
	v_bitop3_b32 v11, v12, v13, 4 bitop3:0x36
	v_bitop3_b32 v16, v14, v0, 7 bitop3:0x78
	v_lshlrev_b32_e32 v25, 4, v11
	v_bitop3_b32 v11, v12, v13, 6 bitop3:0x36
	v_bitop3_b32 v0, v15, v0, 15 bitop3:0x78
	v_lshl_add_u64 v[58:59], s[14:15], 0, v[50:51]
	v_lshlrev_b32_e32 v50, 4, v13
	v_lshlrev_b32_e32 v13, 4, v11
	v_or_b32_e32 v11, 8, v14
	v_lshlrev_b32_e32 v86, 4, v0
	v_bitop3_b32 v0, v15, v56, 4 bitop3:0x36
	v_or_b32_e32 v17, 4, v15
	v_lshl_add_u32 v21, v16, 4, s3
	v_lshlrev_b32_e32 v26, 7, v14
	v_lshlrev_b32_e32 v12, 6, v14
	v_lshlrev_b32_e32 v27, 7, v11
	v_lshlrev_b32_e32 v14, 6, v11
	v_lshlrev_b32_e32 v87, 4, v0
	v_or_b32_e32 v0, 8, v15
	v_bitop3_b32 v11, v15, v56, 8 bitop3:0x36
	v_bitop3_b32 v16, v15, v56, 12 bitop3:0x36
	v_lshlrev_b32_e32 v83, 2, v15
	v_add_u32_e32 v84, 0x80, v18
	v_lshl_add_u64 v[60:61], s[10:11], 0, v[50:51]
	v_lshlrev_b32_e32 v50, 4, v56
	v_lshlrev_b32_e32 v88, 4, v11
	v_or_b32_e32 v11, 12, v15
	v_lshlrev_b32_e32 v89, 4, v16
	v_lshl_add_u32 v28, v15, 8, s3
	v_lshlrev_b32_e32 v16, 6, v15
	v_lshl_add_u32 v15, v17, 8, s3
	v_lshlrev_b32_e32 v18, 6, v17
	v_lshl_add_u32 v17, v0, 8, s3
	v_lshlrev_b32_e32 v20, 6, v0
	v_add_u32_e32 v0, v1, v10
	v_lshl_add_u64 v[62:63], s[8:9], 0, v[50:51]
	s_lshl_b32 s8, s53, 1
	v_lshl_or_b32 v50, s2, 19, v0
	v_mov_b32_e32 v76, v50
	s_mov_b64 s[46:47], 0x2000
	v_lshl_add_u32 v85, v56, 8, s3
	v_lshl_add_u32 v29, v11, 8, s3
	v_lshlrev_b32_e32 v22, 6, v11
	s_add_i32 s3, s55, s8
	v_lshl_add_u64 v[10:11], v[50:51], 0, s[46:47]
	v_or_b32_e32 v82, s52, v56
	s_add_i32 s56, s8, 2
	s_sub_i32 s57, 0, s3
	v_lshl_add_u64 v[0:1], s[4:5], 0, v[10:11]
	v_lshl_add_u64 v[64:65], s[6:7], 0, v[10:11]
	s_mov_b32 s58, 0x40c00000
	s_mov_b32 s36, 0x3c003c00
	v_mov_b32_e32 v116, s36
	v_mov_b32_e32 v117, s36
	v_mov_b32_e32 v118, s36
	v_mov_b32_e32 v119, s36
	v_add_u32_e32 v90, v19, v23
	v_add_u32_e32 v91, v19, v24
	v_add_u32_e32 v92, v19, v25
	v_add_u32_e32 v93, v19, v13
	v_add_u32_e32 v94, v21, v26
	v_lshlrev_b32_e32 v50, 1, v12
	v_add_u32_e32 v95, v21, v27
	v_lshlrev_b32_e32 v66, 1, v14
	v_add_u32_e32 v96, v28, v86
	v_lshlrev_b32_e32 v68, 2, v16
	v_add_u32_e32 v97, v15, v87
	v_lshlrev_b32_e32 v70, 2, v18
	v_add_u32_e32 v98, v17, v88
	v_lshlrev_b32_e32 v72, 2, v20
	v_add_u32_e32 v99, v29, v89
	v_lshlrev_b32_e32 v74, 2, v22
	v_mov_b32_e32 v100, 0xff800000
	v_mov_b32_e32 v101, 0xf149f2ca
	s_mov_b32 s59, s41
	s_branch .LBB2_3

.LBB2_3:
	s_lshl_b32 s63, s53, 1
	s_add_i32 s61, s63, 2
	s_sub_i32 s2, s61, s40
	s_lshl_b32 s60, s53, 7
	s_min_i32 s62, s33, s2
	s_cmp_lt_i32 s2, 1
	s_waitcnt vmcnt(0)
	s_barrier
	s_cbranch_scc1 .LBB2_21
	s_add_i32 s63, s63, s55
	v_lshl_or_b32 v11, s63, 6, v83
	v_add_u32_e32 v10, s60, v82
	v_or_b32_e32 v12, 2, v11
	v_cmp_gt_i32_e64 s[6:7], v12, v10
	v_or_b32_e32 v12, 3, v11
	v_cmp_gt_i32_e64 s[8:9], v12, v10
	v_or_b32_e32 v12, 16, v11
	v_cmp_gt_i32_e64 s[10:11], v12, v10
	v_or_b32_e32 v12, 17, v11
	v_cmp_gt_i32_e64 s[12:13], v12, v10
	v_or_b32_e32 v12, 18, v11
	v_cmp_gt_i32_e64 s[14:15], v12, v10
	v_or_b32_e32 v12, 19, v11
	v_cmp_gt_i32_e64 s[16:17], v12, v10
	v_or_b32_e32 v12, 32, v11
	v_cmp_gt_i32_e64 s[18:19], v12, v10
	v_or_b32_e32 v12, 33, v11
	v_cmp_gt_i32_e64 s[20:21], v12, v10
	v_or_b32_e32 v12, 34, v11
	v_cmp_gt_i32_e64 s[22:23], v12, v10
	v_or_b32_e32 v12, 35, v11
	v_cmp_gt_i32_e64 s[24:25], v12, v10
	v_or_b32_e32 v12, 48, v11
	s_sub_i32 s37, s56, s40
	v_cmp_gt_i32_e64 s[26:27], v12, v10
	v_or_b32_e32 v12, 49, v11
	s_min_i32 s37, s33, s37
	v_cmp_gt_i32_e64 s[2:3], v11, v10
	v_cmp_lt_i32_e64 s[4:5], v11, v10
	v_cmp_gt_i32_e64 s[28:29], v12, v10
	v_or_b32_e32 v12, 50, v11
	v_or_b32_e32 v11, 51, v11
	s_max_i32 s37, s37, 1
	s_lshl_b64 s[38:39], s[40:41], 13
	v_mov_b32_e32 v67, 0
	v_cmp_gt_i32_e64 s[30:31], v12, v10
	v_cmp_gt_i32_e64 s[34:35], v11, v10
	s_mov_b32 s64, 1
	s_sub_i32 s65, 0, s37
	s_add_i32 s66, s40, s57
	s_add_u32 s68, s70, s38
	s_addc_u32 s69, s71, s39
	s_add_u32 s74, s72, s38
	s_addc_u32 s75, s73, s39
	v_mov_b32_e32 v14, v51
	v_mov_b32_e32 v15, v51
	v_mov_b32_e32 v16, v51
	v_mov_b32_e32 v17, v51
	s_mov_b64 s[38:39], -1
	v_mov_b32_e32 v30, 0
	v_mov_b32_e32 v31, v67
	v_mov_b32_e32 v32, v67
	v_mov_b32_e32 v33, v67
	v_mov_b32_e32 v26, 0
	v_mov_b32_e32 v27, v67
	v_mov_b32_e32 v28, v67
	v_mov_b32_e32 v29, v67
	v_mov_b32_e32 v22, v67
	v_mov_b32_e32 v23, v67
	v_mov_b32_e32 v24, v67
	v_mov_b32_e32 v25, v67
	v_mov_b32_e32 v18, v67
	v_mov_b32_e32 v19, v67
	v_mov_b32_e32 v20, v67
	v_mov_b32_e32 v21, v67
	v_mov_b32_e32 v10, v67
	v_mov_b32_e32 v11, v67
	v_mov_b32_e32 v12, v67
	v_mov_b32_e32 v13, v67
	s_branch .LBB2_7
.LBB2_5:
	v_exp_f32_e32 v69, v46
	v_exp_f32_e32 v71, v47
	v_exp_f32_e32 v80, v42
	v_exp_f32_e32 v102, v43
	v_exp_f32_e32 v46, v44
	v_exp_f32_e32 v47, v45
	ds_read_b128 v[42:45], v114 offset:8192
	v_exp_f32_e32 v73, v48
	v_exp_f32_e32 v75, v49
	v_exp_f32_e32 v106, v38
	v_exp_f32_e32 v107, v39
	v_exp_f32_e32 v109, v40
	v_exp_f32_e32 v110, v41
	v_cvt_pk_f16_f32 v41, v46, v47
	v_cvt_pk_f16_f32 v40, v80, v102
	v_cvt_pk_f16_f32 v39, v73, v75
	v_cvt_pk_f16_f32 v38, v69, v71
	ds_read_b128 v[46:49], v114 offset:10240
	ds_read_b128 v[102:105], v114 offset:12288
	s_waitcnt lgkmcnt(0)
	v_mfma_f32_16x16x32_f16 v[26:29], v[42:45], v[38:41], v[26:29]
	ds_read_b128 v[42:45], v114 offset:14336
	v_exp_f32_e32 v34, v34
	v_mfma_f32_16x16x32_f16 v[22:25], v[46:49], v[38:41], v[22:25]
	ds_read_b128 v[46:49], v115 offset:8192
	v_exp_f32_e32 v36, v36
	v_exp_f32_e32 v37, v37
	s_waitcnt lgkmcnt(0)
	v_mfma_f32_16x16x32_f16 v[10:13], v[42:45], v[38:41], v[10:13]
	ds_read_b128 v[42:45], v115 offset:12288
	v_exp_f32_e32 v35, v35
	v_cvt_pk_f16_f32 v37, v36, v37
	v_mfma_f32_16x16x32_f16 v[18:21], v[102:105], v[38:41], v[18:21]
	s_nop 0
	v_cvt_pk_f16_f32 v36, v34, v35
	v_cvt_pk_f16_f32 v35, v109, v110
	v_cvt_pk_f16_f32 v34, v106, v107
	s_mov_b64 s[38:39], 0
	ds_read_b128 v[102:105], v115 offset:10240
	v_mfma_f32_16x16x32_f16 v[26:29], v[46:49], v[34:37], v[26:29]
	ds_read_b128 v[46:49], v115 offset:14336
	s_waitcnt lgkmcnt(0)
	v_mfma_f32_16x16x32_f16 v[18:21], v[42:45], v[34:37], v[18:21]
	v_mfma_f32_16x16x32_f16 v[22:25], v[102:105], v[34:37], v[22:25]
	v_mfma_f32_16x16x32_f16 v[14:17], v[116:119], v[38:41], v[14:17]
	v_mfma_f32_16x16x32_f16 v[10:13], v[46:49], v[34:37], v[10:13]
	v_mfma_f32_16x16x32_f16 v[14:17], v[116:119], v[34:37], v[14:17]
.LBB2_6:
	s_add_i32 s64, s64, 1
	s_add_u32 s68, s68, 0x2000
	s_addc_u32 s69, s69, 0
	s_add_u32 s74, s74, 0x2000
	s_addc_u32 s75, s75, 0
	s_add_i32 s37, s65, s64
	s_cmp_eq_u32 s37, 1
	s_waitcnt vmcnt(0) lgkmcnt(0)
	s_barrier
	s_cbranch_scc1 .LBB2_20
.LBB2_7:
	s_add_i32 s37, s64, -1
	s_and_b32 s37, s37, 1
	s_lshl_b32 s37, s37, 14
	s_add_i32 s48, s40, s64
	s_add_i32 s48, s48, -1
	s_cmp_gt_u32 s48, s63
	s_cbranch_scc1 .Lattn_skip_tile
	v_or_b32_e32 v114, s37, v57
	v_or_b32_e32 v115, s37, v81
	ds_read_b128 v[34:37], v114
	ds_read_b128 v[38:41], v114 offset:2048
	ds_read_b128 v[42:45], v114 offset:4096
	ds_read_b128 v[110:113], v115 offset:2048
	ds_read_b128 v[46:49], v114 offset:6144
	s_cmp_ge_i32 s64, s62
	s_cbranch_scc1 .Lattn_no_dma
	s_xor_b32 s48, s37, 0x4000
	s_add_i32 s48, s50, s48
	s_mov_b32 m0, s48
	s_nop 0
	global_load_lds_dwordx4 v76, s[68:69]
	s_add_i32 m0, s48, 0x2000
	s_nop 0
	global_load_lds_dwordx4 v76, s[74:75]
.Lattn_no_dma:
	s_add_i32 s48, s66, s64
	s_cmp_lg_u32 s48, 1
	s_waitcnt lgkmcnt(4)
	v_mfma_f32_16x16x32_f16 v[34:37], v[34:37], v[6:9], v[30:33]
	s_waitcnt lgkmcnt(2)
	v_mfma_f32_16x16x32_f16 v[102:105], v[42:45], v[6:9], v[30:33]
	ds_read_b128 v[42:45], v115
	v_mfma_f32_16x16x32_f16 v[38:41], v[38:41], v[6:9], v[30:33]
	s_waitcnt lgkmcnt(1)
	v_mfma_f32_16x16x32_f16 v[106:109], v[46:49], v[6:9], v[30:33]
	s_waitcnt lgkmcnt(0)
	v_mfma_f32_16x16x32_f16 v[46:49], v[42:45], v[2:5], v[34:37]
	s_nop 2
	ds_read_b128 v[34:37], v115 offset:4096
	v_mfma_f32_16x16x32_f16 v[42:45], v[110:113], v[2:5], v[38:41]
	ds_read_b128 v[110:113], v115 offset:6144
	s_waitcnt lgkmcnt(0)
	v_mfma_f32_16x16x32_f16 v[38:41], v[34:37], v[2:5], v[102:105]
	v_mfma_f32_16x16x32_f16 v[34:37], v[110:113], v[2:5], v[106:109]
	s_cbranch_scc1 .LBB2_12
	v_cndmask_b32_e64 v69, v46, v100, s[2:3]
	v_cndmask_b32_e64 v46, v69, v46, s[4:5]
	v_cndmask_b32_e64 v47, v100, v47, s[4:5]
	v_cndmask_b32_e64 v48, v48, v100, s[6:7]
	v_cndmask_b32_e64 v49, v49, v100, s[8:9]
	v_cndmask_b32_e64 v42, v42, v100, s[10:11]
	v_cndmask_b32_e64 v43, v43, v100, s[12:13]
	v_cndmask_b32_e64 v44, v44, v100, s[14:15]
	v_cndmask_b32_e64 v45, v45, v100, s[16:17]
	v_cndmask_b32_e64 v38, v38, v100, s[18:19]
	v_cndmask_b32_e64 v39, v39, v100, s[20:21]
	v_cndmask_b32_e64 v40, v40, v100, s[22:23]
	v_cndmask_b32_e64 v41, v41, v100, s[24:25]
	v_cndmask_b32_e64 v34, v34, v100, s[26:27]
	v_cndmask_b32_e64 v35, v35, v100, s[28:29]
	v_cndmask_b32_e64 v36, v36, v100, s[30:31]
	v_cndmask_b32_e64 v37, v37, v100, s[34:35]
.LBB2_12:
	v_max3_f32 v69, v46, v47, v48
	s_and_b64 vcc, exec, s[38:39]
	s_nop 1
	v_max3_f32 v69, v69, v49, v42
	v_max3_f32 v69, v69, v43, v44
	v_max3_f32 v69, v69, v45, v38
	v_max3_f32 v69, v69, v39, v40
	v_max3_f32 v69, v69, v41, v34
	v_max3_f32 v69, v69, v35, v36
	v_max_f32_e32 v69, v69, v37
	v_mov_b32_e32 v71, v69
	s_nop 1
	v_permlane16_swap_b32_e32 v69, v71
	v_max_f32_e32 v69, v69, v71
	v_mov_b32_e32 v71, v69
	s_nop 1
	v_permlane32_swap_b32_e32 v69, v71
	v_max_f32_e32 v69, v69, v71
	s_cbranch_vccnz .Lattn_first_tile
	v_cmp_lt_f32_e32 vcc, s58, v69
	s_nop 1
	s_cbranch_vccz .LBB2_5
	v_max_f32_e32 v71, v69, v69
	v_max_f32_e32 v80, 0, v71
	s_branch .Lattn_rescale
.Lattn_first_tile:
	v_mov_b32_e32 v80, v69
.Lattn_rescale:
	v_exp_f32_e64 v32, -v80
	v_add_f32_e32 v67, v67, v80
	v_xor_b32_e32 v30, 0x80000000, v67
	v_pk_add_f32 v[46:47], v[46:47], v[80:81] op_sel_hi:[1,0] neg_lo:[0,1] neg_hi:[0,1]
	v_pk_add_f32 v[48:49], v[48:49], v[80:81] op_sel_hi:[1,0] neg_lo:[0,1] neg_hi:[0,1]
	v_pk_add_f32 v[42:43], v[42:43], v[80:81] op_sel_hi:[1,0] neg_lo:[0,1] neg_hi:[0,1]
	v_pk_add_f32 v[44:45], v[44:45], v[80:81] op_sel_hi:[1,0] neg_lo:[0,1] neg_hi:[0,1]
	v_pk_add_f32 v[38:39], v[38:39], v[80:81] op_sel_hi:[1,0] neg_lo:[0,1] neg_hi:[0,1]
	v_pk_add_f32 v[40:41], v[40:41], v[80:81] op_sel_hi:[1,0] neg_lo:[0,1] neg_hi:[0,1]
	v_pk_add_f32 v[34:35], v[34:35], v[80:81] op_sel_hi:[1,0] neg_lo:[0,1] neg_hi:[0,1]
	v_pk_mul_f32 v[12:13], v[32:33], v[12:13] op_sel_hi:[0,1]
	v_pk_mul_f32 v[10:11], v[32:33], v[10:11] op_sel_hi:[0,1]
	v_pk_mul_f32 v[20:21], v[32:33], v[20:21] op_sel_hi:[0,1]
	v_pk_mul_f32 v[18:19], v[32:33], v[18:19] op_sel_hi:[0,1]
	v_pk_mul_f32 v[24:25], v[32:33], v[24:25] op_sel_hi:[0,1]
	v_pk_mul_f32 v[22:23], v[32:33], v[22:23] op_sel_hi:[0,1]
	v_pk_mul_f32 v[28:29], v[32:33], v[28:29] op_sel_hi:[0,1]
	v_pk_mul_f32 v[26:27], v[32:33], v[26:27] op_sel_hi:[0,1]
	v_pk_add_f32 v[36:37], v[36:37], v[80:81] op_sel_hi:[1,0] neg_lo:[0,1] neg_hi:[0,1]
	v_pk_mul_f32 v[16:17], v[16:17], v[32:33] op_sel_hi:[1,0]
	v_pk_mul_f32 v[14:15], v[14:15], v[32:33] op_sel_hi:[1,0]
	v_mov_b32_e32 v31, v30
	v_mov_b32_e32 v32, v30
	v_mov_b32_e32 v33, v30
	s_branch .LBB2_5
.Lattn_skip_tile:
	s_cmp_ge_i32 s64, s62
	s_cbranch_scc1 .LBB2_6
	s_xor_b32 s48, s37, 0x4000
	s_add_i32 s48, s50, s48
	s_mov_b32 m0, s48
	s_nop 0
	global_load_lds_dwordx4 v76, s[68:69]
	s_add_i32 m0, s48, 0x2000
	s_nop 0
	global_load_lds_dwordx4 v76, s[74:75]
	s_branch .LBB2_6

	.amdhsa_kernel _Z11attn_kernelPKDF16_S0_S0_PfPDF16_S1_
		.amdhsa_group_segment_fixed_size 65536
		.amdhsa_private_segment_fixed_size 0
		.amdhsa_kernarg_size 48
		.amdhsa_user_sgpr_count 2
		.amdhsa_user_sgpr_dispatch_ptr 0
		.amdhsa_user_sgpr_queue_ptr 0
		.amdhsa_user_sgpr_kernarg_segment_ptr 1
		.amdhsa_user_sgpr_dispatch_id 0
		.amdhsa_user_sgpr_kernarg_preload_length 0
		.amdhsa_user_sgpr_kernarg_preload_offset 0
		.amdhsa_user_sgpr_private_segment_size 0
		.amdhsa_uses_dynamic_stack 0
		.amdhsa_enable_private_segment 0
		.amdhsa_system_sgpr_workgroup_id_x 1
		.amdhsa_system_sgpr_workgroup_id_y 0
		.amdhsa_system_sgpr_workgroup_id_z 0
		.amdhsa_system_sgpr_workgroup_info 0
		.amdhsa_system_vgpr_workitem_id 0
		.amdhsa_next_free_vgpr 120
		.amdhsa_next_free_sgpr 96
		.amdhsa_accum_offset 120
		.amdhsa_reserve_vcc 1
		.amdhsa_float_round_mode_32 0
		.amdhsa_float_round_mode_16_64 0
		.amdhsa_float_denorm_mode_32 3
		.amdhsa_float_denorm_mode_16_64 3
		.amdhsa_dx10_clamp 1
		.amdhsa_ieee_mode 1
		.amdhsa_fp16_overflow 0
		.amdhsa_tg_split 0
		.amdhsa_exception_fp_ieee_invalid_op 0
		.amdhsa_exception_fp_denorm_src 0
		.amdhsa_exception_fp_ieee_div_zero 0
		.amdhsa_exception_fp_ieee_overflow 0
		.amdhsa_exception_fp_ieee_underflow 0
		.amdhsa_exception_fp_ieee_inexact 0
		.amdhsa_exception_int_div_zero 0
	.end_amdhsa_kernel

amdhsa.kernels:
  - .agpr_count:     0
    .args:
      - .actual_access:  read_only
        .address_space:  global
        .offset:         0
        .size:           8
        .value_kind:     global_buffer
      - .actual_access:  read_only
        .address_space:  global
        .offset:         8
        .size:           8
        .value_kind:     global_buffer
      - .actual_access:  read_only
        .address_space:  global
        .offset:         16
        .size:           8
        .value_kind:     global_buffer
      - .actual_access:  write_only
        .address_space:  global
        .offset:         24
        .size:           8
        .value_kind:     global_buffer
      - .offset:         32
        .size:           4
        .value_kind:     hidden_block_count_x
      - .offset:         36
        .size:           4
        .value_kind:     hidden_block_count_y
      - .offset:         40
        .size:           4
        .value_kind:     hidden_block_count_z
      - .offset:         44
        .size:           2
        .value_kind:     hidden_group_size_x
      - .offset:         46
        .size:           2
        .value_kind:     hidden_group_size_y
      - .offset:         48
        .size:           2
        .value_kind:     hidden_group_size_z
      - .offset:         50
        .size:           2
        .value_kind:     hidden_remainder_x
      - .offset:         52
        .size:           2
        .value_kind:     hidden_remainder_y
      - .offset:         54
        .size:           2
        .value_kind:     hidden_remainder_z
      - .offset:         72
        .size:           8
        .value_kind:     hidden_global_offset_x
      - .offset:         80
        .size:           8
        .value_kind:     hidden_global_offset_y
      - .offset:         88
        .size:           8
        .value_kind:     hidden_global_offset_z
      - .offset:         96
        .size:           2
        .value_kind:     hidden_grid_dims
    .group_segment_fixed_size: 0
    .kernarg_segment_align: 8
    .kernarg_segment_size: 288
    .language:       OpenCL C
    .language_version:
      - 2
      - 0
    .max_flat_workgroup_size: 1024
    .name:           _Z13prep_w_kernelPKfS0_S0_PDv8_DF16_
    .private_segment_fixed_size: 0
    .sgpr_count:     18
    .sgpr_spill_count: 0
    .symbol:         _Z13prep_w_kernelPKfS0_S0_PDv8_DF16_.kd
    .uniform_work_group_size: 1
    .uses_dynamic_stack: false
    .vgpr_count:     15
    .vgpr_spill_count: 0
    .wavefront_size: 64
  - .agpr_count:     0
    .args:
      - .actual_access:  read_only
        .address_space:  global
        .offset:         0
        .size:           8
        .value_kind:     global_buffer
      - .actual_access:  read_only
        .address_space:  global
        .offset:         8
        .size:           8
        .value_kind:     global_buffer
      - .actual_access:  write_only
        .address_space:  global
        .offset:         16
        .size:           8
        .value_kind:     global_buffer
      - .actual_access:  write_only
        .address_space:  global
        .offset:         24
        .size:           8
        .value_kind:     global_buffer
      - .actual_access:  write_only
        .address_space:  global
        .offset:         32
        .size:           8
        .value_kind:     global_buffer
    .group_segment_fixed_size: 131072
    .kernarg_segment_align: 8
    .kernarg_segment_size: 40
    .language:       OpenCL C
    .language_version:
      - 2
      - 0
    .max_flat_workgroup_size: 512
    .name:           _Z11proj_kernelPKfPKDv8_DF16_PDF16_S4_S4_
    .private_segment_fixed_size: 0
    .sgpr_count:     26
    .sgpr_spill_count: 0
    .symbol:         _Z11proj_kernelPKfPKDv8_DF16_PDF16_S4_S4_.kd
    .uniform_work_group_size: 1
    .uses_dynamic_stack: false
    .vgpr_count:     158
    .vgpr_spill_count: 0
    .wavefront_size: 64
  - .agpr_count:     0
    .args:
      - .actual_access:  read_only
        .address_space:  global
        .offset:         0
        .size:           8
        .value_kind:     global_buffer
      - .address_space:  global
        .offset:         8
        .size:           8
        .value_kind:     global_buffer
      - .address_space:  global
        .offset:         16
        .size:           8
        .value_kind:     global_buffer
      - .actual_access:  write_only
        .address_space:  global
        .offset:         24
        .size:           8
        .value_kind:     global_buffer
      - .actual_access:  write_only
        .address_space:  global
        .offset:         32
        .size:           8
        .value_kind:     global_buffer
      - .actual_access:  write_only
        .address_space:  global
        .offset:         40
        .size:           8
        .value_kind:     global_buffer
    .group_segment_fixed_size: 65536
    .kernarg_segment_align: 8
    .kernarg_segment_size: 48
    .language:       OpenCL C
    .language_version:
      - 2
      - 0
    .max_flat_workgroup_size: 512
    .name:           _Z11attn_kernelPKDF16_S0_S0_PfPDF16_S1_
    .private_segment_fixed_size: 0
    .sgpr_count:     82
    .sgpr_spill_count: 0
    .symbol:         _Z11attn_kernelPKDF16_S0_S0_PfPDF16_S1_.kd
    .uniform_work_group_size: 1
    .uses_dynamic_stack: false
    .vgpr_count:     120
    .vgpr_spill_count: 0
    .wavefront_size: 64
  - .agpr_count:     0
    .args:
      - .actual_access:  read_only
        .address_space:  global
        .offset:         0
        .size:           8
        .value_kind:     global_buffer
      - .actual_access:  read_only
        .address_space:  global
        .offset:         8
        .size:           8
        .value_kind:     global_buffer
      - .actual_access:  write_only
        .address_space:  global
        .offset:         16
        .size:           8
        .value_kind:     global_buffer
    .group_segment_fixed_size: 0
    .kernarg_segment_align: 8
    .kernarg_segment_size: 24
    .language:       OpenCL C
    .language_version:
      - 2
      - 0
    .max_flat_workgroup_size: 256
    .name:           _Z14combine_kernelPKDF16_PKfPf
    .private_segment_fixed_size: 0
    .sgpr_count:     70
    .sgpr_spill_count: 0
    .symbol:         _Z14combine_kernelPKDF16_PKfPf.kd
    .uniform_work_group_size: 1
    .uses_dynamic_stack: false
    .vgpr_count:     46
    .vgpr_spill_count: 0
    .wavefront_size: 64
